# flat-release grid barrier at all 12 sites: each XCD leader (after its L2 writeback) adds its XCD workgroup count to every per-XCD release word, everyone polls own word >= 256*(gen+1); removes TOP coun
# speedup vs baseline: 1.0097x; 1.0022x over previous
.LBB0_69:
	s_lshl_b32 s4, s33, 8
	s_add_u32 s4, s14, s4
	s_addc_u32 s5, s15, 0
	v_mov_b32_e32 v2, 0x1000
	v_mov_b32_e32 v4, 1
	global_atomic_add v4, v2, v4, s[4:5] offset:1024 sc0
	buffer_inv sc1
	v_cvt_f32_u32_e32 v2, v3
	v_sub_u32_e32 v5, 0, v3
	v_rcp_iflag_f32_e32 v2, v2
	s_nop 0
	v_mul_f32_e32 v2, 0x4f7ffffe, v2
	v_cvt_u32_f32_e32 v2, v2
	v_mul_lo_u32 v5, v5, v2
	v_mul_hi_u32 v5, v2, v5
	v_add_u32_e32 v2, v2, v5
	s_waitcnt vmcnt(1)
	v_mul_hi_u32 v2, v4, v2
	v_mul_lo_u32 v5, v2, v3
	v_sub_u32_e32 v5, v4, v5
	v_add_u32_e32 v6, 1, v2
	v_cmp_ge_u32_e32 vcc, v5, v3
	v_add_u32_e32 v4, 1, v4
	s_nop 0
	v_cndmask_b32_e32 v2, v2, v6, vcc
	v_sub_u32_e32 v6, v5, v3
	v_cndmask_b32_e32 v5, v5, v6, vcc
	v_add_u32_e32 v6, 1, v2
	v_cmp_ge_u32_e32 vcc, v5, v3
	s_nop 1
	v_cndmask_b32_e32 v2, v2, v6, vcc
	v_mul_lo_u32 v5, v3, v2
	v_add_u32_e32 v3, v5, v3
	v_cmp_ne_u32_e32 vcc, v4, v3
	v_sub_u32_e32 v6, v3, v5
	s_waitcnt lgkmcnt(0)
	v_mov_b32_e32 v1, 0
	v_add_u32_e32 v2, 1, v2
	v_lshlrev_b32_e32 v2, 8, v2
	s_add_u32 s8, s4, 0x2400
	s_addc_u32 s9, s5, 0
	s_waitcnt lgkmcnt(0)
	s_cbranch_vccnz .Lnb_poll_99
	buffer_wbl2 sc1
	s_add_u32 s12, s16, 0x6400
	s_addc_u32 s13, s17, 0
	s_mov_b32 s10, 16
	s_waitcnt vmcnt(0)
.Lnb_loop_99:
	global_atomic_add v1, v6, s[12:13]
	s_add_u32 s12, s12, 0x100
	s_addc_u32 s13, s13, 0
	s_sub_u32 s10, s10, 1
	s_cmp_lg_u32 s10, 0
	s_cbranch_scc1 .Lnb_loop_99
.Lnb_poll_99:
	s_mov_b32 s10, 0
	s_nop 4
.Lnb_spin_99:
	global_load_dword v3, v1, s[8:9] sc1
	s_waitcnt vmcnt(0)
	v_sub_u32_e32 v3, v3, v2
	v_cmp_gt_i32_e32 vcc, 0, v3
	s_cbranch_vccz .Lnb_done_99
	s_sleep 1
	s_add_u32 s10, s10, 1
	s_cmp_lt_u32 s10, 0x20000
	s_cbranch_scc1 .Lnb_spin_99
.Lnb_done_99:
.LBB0_101:
	s_or_b64 exec, exec, s[2:3]
	s_waitcnt lgkmcnt(0)
	s_barrier
.LBB0_102:
	s_load_dwordx16 s[36:51], s[0:1], 0x40
	s_add_u32 s30, s16, 0x100000
	s_addc_u32 s31, s17, 0
	s_add_u32 s26, s16, 0x25313200
	s_addc_u32 s27, s17, 0
	s_waitcnt lgkmcnt(0)
	v_writelane_b32 v251, s36, 31
	s_cmpk_lt_i32 s96, 0x80
	s_cselect_b64 s[0:1], -1, 0
	v_writelane_b32 v251, s37, 32
	v_writelane_b32 v251, s38, 33
	v_writelane_b32 v251, s39, 34
	v_writelane_b32 v251, s40, 35
	v_writelane_b32 v251, s41, 36
	v_writelane_b32 v251, s42, 37
	v_writelane_b32 v251, s43, 38
	v_writelane_b32 v251, s44, 39
	v_writelane_b32 v251, s45, 40
	v_writelane_b32 v251, s46, 41
	v_writelane_b32 v251, s47, 42
	v_writelane_b32 v251, s48, 43
	v_writelane_b32 v251, s49, 44
	v_writelane_b32 v251, s50, 45
	v_writelane_b32 v251, s51, 46
	v_writelane_b32 v251, s0, 47
	v_mov_b32_e32 v3, 0
	v_mbcnt_lo_u32_b32 v1, -1, 0
	v_writelane_b32 v251, s1, 48
	s_lshr_b32 s0, s96, 31
	s_add_i32 s0, s96, s0
	s_lshl_b32 s1, s0, 6
	s_and_b32 s1, s1, 0xffffff80
	s_and_b32 s0, s0, -2
	s_sub_i32 s2, s96, s0
	v_writelane_b32 v251, s1, 49
	s_add_i32 s0, s1, 0x80
	v_writelane_b32 v251, s0, 50
	s_mov_b32 s0, s2
	s_ashr_i32 s3, s2, 31
	v_writelane_b32 v251, s0, 51
	v_mov_b32_e32 v228, 1
	v_mbcnt_hi_u32_b32 v229, -1, v1
	v_writelane_b32 v251, s1, 52
	s_lshl_b64 s[0:1], s[2:3], 20
	s_add_u32 s0, s26, s0
	s_addc_u32 s1, s27, s1
	s_add_u32 s2, s0, 0x4000
	s_addc_u32 s3, s1, 0
	v_writelane_b32 v251, s2, 53
	v_mov_b32_e32 v230, 0x358637bd
	v_mov_b32_e32 v231, 0x260
	v_writelane_b32 v251, s3, 54
	s_add_u32 s2, s0, 0x8000
	s_addc_u32 s3, s1, 0
	v_writelane_b32 v251, s2, 55
	v_mov_b32_e32 v232, 0x3727c5ac
	v_mov_b64_e32 v[202:203], 0xff
	v_writelane_b32 v251, s3, 56
	s_add_u32 s2, s16, 0x100080
	s_addc_u32 s3, s17, 0
	v_writelane_b32 v251, s2, 57
	v_mov_b32_e32 v233, 0x41b17218
	v_mov_b32_e32 v234, 0xf149f2ca
	v_writelane_b32 v251, s3, 58
	s_add_u32 s2, s0, 0xc000
	v_writelane_b32 v251, s0, 59
	s_addc_u32 s3, s1, 0
	v_mov_b32_e32 v235, 0x2200
	v_writelane_b32 v251, s1, 60
	v_writelane_b32 v251, s2, 61
	s_add_u32 s0, s16, 0x6102200
	s_addc_u32 s1, s17, 0
	v_writelane_b32 v251, s3, 62
	v_writelane_b32 v251, s0, 63
	v_mov_b32_e32 v84, v3
	v_mov_b32_e32 v85, v3
	v_writelane_b32 v252, s1, 0
	s_add_u32 s0, s16, 0x25514300
	v_writelane_b32 v252, s0, 1
	s_addc_u32 s0, s17, 0
	s_cmpk_lt_i32 s66, 0x100
	v_writelane_b32 v252, s0, 2
	s_cselect_b64 s[0:1], -1, 0
	v_writelane_b32 v252, s0, 3
	v_mov_b32_e32 v86, v3
	v_mov_b32_e32 v87, v3
	v_writelane_b32 v252, s1, 4
	s_ashr_i32 s0, s66, 31
	v_writelane_b32 v252, s0, 5
	s_lshr_b32 s0, s0, 29
	s_add_i32 s0, s66, s0
	s_ashr_i32 s2, s0, 3
	s_and_b32 s0, s0, -8
	s_sub_i32 s3, s66, s0
	s_lshl_b32 s4, s3, 5
	s_add_u32 s0, s16, 0x4200
	s_addc_u32 s1, s17, 0
	v_writelane_b32 v252, s0, 6
	v_mov_b32_e32 v236, 0x2000880
	v_mov_b32_e32 v237, 0x1000
	v_writelane_b32 v252, s1, 7
	s_add_u32 s0, s16, 0x4400
	s_addc_u32 s1, s17, 0
	v_writelane_b32 v252, s0, 8
	v_mov_b32_e32 v238, 0x1800
	s_movk_i32 s29, 0x80
	v_writelane_b32 v252, s1, 9
	s_add_u32 s0, s16, 0x4500
	s_addc_u32 s1, s17, 0
	v_writelane_b32 v252, s0, 10
	s_mov_b32 s90, 0
	s_mov_b32 s35, 0
	v_writelane_b32 v252, s1, 11
	s_add_u32 s0, s16, 0x4600
	s_addc_u32 s1, s17, 0
	v_writelane_b32 v252, s0, 12
	s_mov_b64 s[36:37], 0x80
	s_mov_b32 s46, 0x3e38aa3b
	v_writelane_b32 v252, s1, 13
	s_add_u32 s0, s16, 0x4700
	s_addc_u32 s1, s17, 0
	v_writelane_b32 v252, s0, 14
	s_mov_b32 s28, 0x3fd744fd
	s_nop 0
	v_writelane_b32 v252, s1, 15
	s_add_u32 s0, s16, 0x4800
	s_addc_u32 s1, s17, 0
	v_writelane_b32 v252, s0, 16
	s_nop 1
	v_writelane_b32 v252, s1, 17
	s_add_u32 s0, s16, 0x4900
	s_addc_u32 s1, s17, 0
	v_writelane_b32 v252, s0, 18
	s_nop 1
	v_writelane_b32 v252, s1, 19
	s_add_u32 s0, s16, 0x4a00
	s_addc_u32 s1, s17, 0
	v_writelane_b32 v252, s0, 20
	s_nop 1
	v_writelane_b32 v252, s1, 21
	s_add_u32 s0, s16, 0x4b00
	s_addc_u32 s1, s17, 0
	v_writelane_b32 v252, s0, 22
	s_nop 1
	v_writelane_b32 v252, s1, 23
	s_add_u32 s0, s16, 0x4c00
	s_addc_u32 s1, s17, 0
	v_writelane_b32 v252, s0, 24
	s_nop 1
	v_writelane_b32 v252, s1, 25
	s_add_u32 s0, s16, 0x4d00
	s_addc_u32 s1, s17, 0
	v_writelane_b32 v252, s0, 26
	s_nop 1
	v_writelane_b32 v252, s1, 27
	s_add_u32 s0, s16, 0x4e00
	s_addc_u32 s1, s17, 0
	v_writelane_b32 v252, s0, 28
	s_nop 1
	v_writelane_b32 v252, s1, 29
	s_add_u32 s0, s16, 0x4f00
	s_addc_u32 s1, s17, 0
	v_writelane_b32 v252, s0, 30
	s_nop 1
	v_writelane_b32 v252, s1, 31
	s_add_u32 s0, s16, 0x5000
	s_addc_u32 s1, s17, 0
	v_writelane_b32 v252, s0, 32
	s_nop 1
	v_writelane_b32 v252, s1, 33
	s_add_u32 s0, s16, 0x5100
	s_addc_u32 s1, s17, 0
	v_writelane_b32 v252, s0, 34
	s_nop 1
	v_writelane_b32 v252, s1, 35
	s_add_u32 s0, s16, 0x5200
	s_addc_u32 s1, s17, 0
	v_writelane_b32 v252, s0, 36
	s_nop 1
	v_writelane_b32 v252, s1, 37
	s_add_u32 s0, s16, 0x5300
	s_addc_u32 s1, s17, 0
	v_writelane_b32 v252, s0, 38
	s_cmp_eq_u32 s33, 15
	s_nop 0
	v_writelane_b32 v252, s1, 39
	s_cselect_b64 s[0:1], -1, 0
	v_writelane_b32 v252, s0, 40
	s_cmp_eq_u32 s33, 14
	s_nop 0
	v_writelane_b32 v252, s1, 41
	s_cselect_b64 s[0:1], -1, 0
	v_writelane_b32 v252, s0, 42
	s_cmp_eq_u32 s33, 13
	s_nop 0
	v_writelane_b32 v252, s1, 43
	s_cselect_b64 s[0:1], -1, 0
	v_writelane_b32 v252, s0, 44
	s_cmp_eq_u32 s33, 12
	s_nop 0
	v_writelane_b32 v252, s1, 45
	s_cselect_b64 s[0:1], -1, 0
	v_writelane_b32 v252, s0, 46
	s_cmp_eq_u32 s33, 11
	s_nop 0
	v_writelane_b32 v252, s1, 47
	s_cselect_b64 s[0:1], -1, 0
	v_writelane_b32 v252, s0, 48
	s_cmp_eq_u32 s33, 10
	s_nop 0
	v_writelane_b32 v252, s1, 49
	s_cselect_b64 s[0:1], -1, 0
	v_writelane_b32 v252, s0, 50
	s_cmp_eq_u32 s33, 9
	s_nop 0
	v_writelane_b32 v252, s1, 51
	s_cselect_b64 s[0:1], -1, 0
	v_writelane_b32 v252, s0, 52
	s_cmp_eq_u32 s33, 8
	s_nop 0
	v_writelane_b32 v252, s1, 53
	s_cselect_b64 s[0:1], -1, 0
	v_writelane_b32 v252, s0, 54
	s_cmp_eq_u32 s33, 7
	s_nop 0
	v_writelane_b32 v252, s1, 55
	s_cselect_b64 s[0:1], -1, 0
	v_writelane_b32 v252, s0, 56
	s_cmp_eq_u32 s33, 6
	s_nop 0
	v_writelane_b32 v252, s1, 57
	s_cselect_b64 s[0:1], -1, 0
	v_writelane_b32 v252, s0, 58
	s_cmp_eq_u32 s33, 5
	s_nop 0
	v_writelane_b32 v252, s1, 59
	s_cselect_b64 s[0:1], -1, 0
	v_writelane_b32 v252, s0, 60
	s_cmp_eq_u32 s33, 4
	s_nop 0
	v_writelane_b32 v252, s1, 61
	s_cselect_b64 s[0:1], -1, 0
	v_writelane_b32 v252, s0, 62
	s_cmp_eq_u32 s33, 3
	s_nop 0
	v_writelane_b32 v252, s1, 63
	s_cselect_b64 s[0:1], -1, 0
	v_writelane_b32 v253, s0, 0
	s_cmp_eq_u32 s33, 2
	s_nop 0
	v_writelane_b32 v253, s1, 1
	s_cselect_b64 s[0:1], -1, 0
	v_writelane_b32 v253, s0, 2
	s_cmp_eq_u32 s33, 1
	s_nop 0
	v_writelane_b32 v253, s1, 3
	s_cselect_b64 s[0:1], -1, 0
	v_writelane_b32 v253, s0, 4
	s_cmp_eq_u32 s33, 0
	s_nop 0
	v_writelane_b32 v253, s1, 5
	s_cselect_b64 s[0:1], -1, 0
	v_writelane_b32 v253, s0, 6
	s_nop 1
	v_writelane_b32 v253, s1, 7
	s_lshl_b32 s0, s33, 8
	s_add_u32 s0, s14, s0
	s_addc_u32 s1, s15, 0
	s_add_u32 s6, s0, 0x1400
	s_addc_u32 s7, s1, 0
	v_writelane_b32 v253, s6, 8
	s_add_u32 s0, s0, 0x2400
	s_addc_u32 s1, s1, 0
	v_writelane_b32 v253, s7, 9
	v_writelane_b32 v253, s0, 10
	s_nop 1
	v_writelane_b32 v253, s1, 11
	s_add_u32 s0, s16, 0x7400
	s_addc_u32 s1, s17, 0
	v_writelane_b32 v253, s0, 12
	s_nop 1
	v_writelane_b32 v253, s1, 13
	s_add_u32 s0, s16, 0x7500
	s_addc_u32 s1, s17, 0
	v_writelane_b32 v253, s0, 14
	s_nop 1
	v_writelane_b32 v253, s1, 15
	s_add_u32 s0, s16, 0x1a10aa00
	s_addc_u32 s1, s17, 0
	v_writelane_b32 v253, s0, 16
	s_nop 1
	v_writelane_b32 v253, s1, 17
	s_add_u32 s0, s16, 0x1a50bb00
	s_addc_u32 s1, s17, 0
	v_writelane_b32 v253, s0, 18
	s_cmpk_lt_i32 s96, 0x100
	s_nop 0
	v_writelane_b32 v253, s1, 19
	s_cselect_b64 s[0:1], -1, 0
	v_writelane_b32 v253, s0, 20
	s_nop 1
	v_writelane_b32 v253, s1, 21
	s_add_u32 s0, s16, 0x16108800
	s_addc_u32 s1, s17, 0
	s_add_u32 s78, s16, 0x18109900
	s_addc_u32 s79, s17, 0
	s_add_u32 s5, s16, 0x26515400
	v_writelane_b32 v253, s5, 22
	s_addc_u32 s5, s17, 0
	s_add_u32 s6, s16, 0x16108880
	v_writelane_b32 v253, s5, 23
	s_addc_u32 s7, s17, 0
	s_add_i32 s5, s20, 0xffffff68
	v_writelane_b32 v253, s6, 24
	s_cmp_lt_i32 s66, s5
	s_nop 0
	v_writelane_b32 v253, s7, 25
	s_cselect_b64 s[6:7], -1, 0
	v_writelane_b32 v253, s6, 26
	s_nop 1
	v_writelane_b32 v253, s7, 27
	v_writelane_b32 v253, s5, 28
	s_sub_i32 s5, s66, s5
	s_lshl_b32 s6, s5, 3
	v_writelane_b32 v253, s6, 29
	s_add_u32 s6, s16, 0x20311000
	v_writelane_b32 v253, s6, 30
	s_addc_u32 s6, s17, 0
	v_writelane_b32 v253, s6, 31
	s_add_u32 s6, s16, 0x24312100
	v_writelane_b32 v253, s6, 32
	s_addc_u32 s6, s17, 0
	v_writelane_b32 v253, s6, 33
	s_add_u32 s6, s16, 0x27516500
	v_writelane_b32 v253, s6, 34
	s_addc_u32 s6, s17, 0
	v_writelane_b32 v253, s6, 35
	s_add_u32 s6, s16, 0x47517600
	v_writelane_b32 v253, s6, 36
	s_addc_u32 s6, s17, 0
	v_writelane_b32 v253, s6, 37
	s_add_u32 s6, s16, 0x5f61ba00
	s_addc_u32 s7, s17, 0
	v_writelane_b32 v253, s6, 38
	s_lshl_b32 s5, s5, 9
	s_cmpk_lt_i32 s66, 0x400
	v_writelane_b32 v253, s7, 39
	v_writelane_b32 v253, s5, 40
	s_cselect_b64 s[6:7], -1, 0
	v_writelane_b32 v253, s6, 41
	s_lshl_b32 s5, s3, 7
	s_nop 0
	v_writelane_b32 v253, s7, 42
	s_add_u32 s6, s16, 0x8103300
	s_addc_u32 s7, s17, 0
	s_add_u32 s10, s16, 0xa104400
	v_writelane_b32 v253, s6, 43
	s_addc_u32 s11, s17, 0
	s_nop 0
	v_writelane_b32 v253, s7, 44
	s_add_u32 s6, s16, 0x12107700
	s_addc_u32 s7, s17, 0
	v_writelane_b32 v253, s6, 45
	s_nop 1
	v_writelane_b32 v253, s7, 46
	s_add_u32 s6, s16, 0x57518700
	s_addc_u32 s7, s17, 0
	v_writelane_b32 v253, s6, 47
	s_nop 1
	v_writelane_b32 v253, s7, 48
	s_add_u32 s6, s16, 0x5f51a900
	s_addc_u32 s7, s17, 0
	v_writelane_b32 v253, s6, 49
	s_cmpk_lt_i32 s96, 0x800
	s_nop 0
	v_writelane_b32 v253, s7, 50
	s_cselect_b64 s[6:7], -1, 0
	v_writelane_b32 v253, s6, 51
	s_lshl_b32 s9, s96, 13
	s_and_b32 s9, s9, 0x3e0000
	v_writelane_b32 v253, s7, 52
	s_lshl_b32 s6, s96, 7
	s_and_b32 s8, s6, 0x780
	s_ashr_i32 s6, s96, 9
	s_ashr_i32 s7, s6, 31
	s_lshl_b64 s[6:7], s[6:7], 22
	s_or_b32 s6, s6, s9
	s_or_b32 s6, s6, s8
	v_writelane_b32 v253, s6, 53
	s_nop 1
	v_writelane_b32 v253, s7, 54
	s_lshl_b64 s[6:7], s[6:7], 1
	v_writelane_b32 v253, s10, 55
	s_add_u32 s6, s10, s6
	v_writelane_b32 v253, s11, 56
	s_addc_u32 s7, s11, s7
	v_writelane_b32 v253, s6, 57
	s_nop 1
	v_writelane_b32 v253, s7, 58
	s_add_u32 s6, s16, 0x5b519800
	s_addc_u32 s7, s17, 0
	v_writelane_b32 v253, s6, 59
	s_nop 1
	v_writelane_b32 v253, s7, 60
	s_lshl_b32 s6, s96, 9
	v_writelane_b32 v253, s6, 61
	s_lshl_b32 s6, s20, 9
	v_writelane_b32 v253, s6, 62
	s_add_u32 s6, s16, 0xc105500
	s_addc_u32 s7, s17, 0
	v_writelane_b32 v253, s6, 63
	s_cmpk_lt_i32 s96, 0x400
	s_nop 0
	v_writelane_b32 v254, s7, 0
	s_cselect_b64 s[6:7], -1, 0
	v_writelane_b32 v254, s6, 1
	s_nop 1
	v_writelane_b32 v254, s7, 2
	s_lshl_b32 s6, s96, 4
	v_writelane_b32 v254, s6, 3
	s_and_b32 s6, s6, 0xf0
	s_and_b32 s7, s96, 0x7fffff00
	s_or_b32 s6, s7, s6
	s_bfe_u32 s7, s96, 0x40004
	s_or_b32 s6, s6, s7
	s_lshl_b32 s6, s6, 1
	s_add_u32 s22, s16, 0x4101100
	s_addc_u32 s23, s17, 0
	v_writelane_b32 v254, s6, 4
	s_add_u32 s6, s16, 0x6381dc00
	s_addc_u32 s7, s17, 0
	v_writelane_b32 v254, s6, 5
	s_nop 1
	v_writelane_b32 v254, s7, 6
	s_add_u32 s6, s16, 0x1a90cc00
	s_addc_u32 s7, s17, 0
	v_writelane_b32 v254, s6, 7
	s_nop 1
	v_writelane_b32 v254, s7, 8
	s_add_u32 s6, s16, 0x1aa0dd00
	s_addc_u32 s7, s17, 0
	v_writelane_b32 v254, s6, 9
	s_lshl_b32 s8, s96, 5
	s_nop 0
	v_writelane_b32 v254, s7, 10
	s_ashr_i32 s6, s20, 31
	s_lshr_b32 s6, s6, 30
	s_add_i32 s6, s20, s6
	s_ashr_i32 s6, s6, 2
	v_writelane_b32 v254, s6, 11
	s_add_u32 s6, s16, 0x10000
	v_writelane_b32 v254, s6, 12
	s_addc_u32 s6, s17, 0
	s_lshl_b32 s7, s20, 1
	v_writelane_b32 v254, s6, 13
	s_add_i32 s9, s96, s7
	v_writelane_b32 v254, s7, 14
	s_ashr_i32 s7, s9, 31
	s_ashr_i32 s6, s96, 31
	s_lshr_b32 s7, s7, 30
	s_lshr_b32 s6, s6, 30
	s_add_i32 s7, s9, s7
	s_add_i32 s6, s96, s6
	v_writelane_b32 v254, s9, 15
	s_ashr_i32 s7, s7, 2
	v_writelane_b32 v254, s7, 16
	s_ashr_i32 s7, s6, 2
	s_add_u32 s24, s16, 0x1ab0ee00
	s_addc_u32 s25, s17, 0
	s_add_u32 s10, s16, 0x6391ed00
	v_writelane_b32 v254, s7, 17
	s_addc_u32 s11, s17, 0
	v_writelane_b32 v254, s10, 18
	s_and_b32 s6, s6, -4
	s_sub_i32 s6, s96, s6
	v_writelane_b32 v254, s11, 19
	v_writelane_b32 v254, s6, 20
	s_add_u32 s6, s16, 0x4101180
	s_addc_u32 s7, s17, 0
	v_writelane_b32 v254, s6, 21
	s_nop 1
	v_writelane_b32 v254, s7, 22
	s_add_u32 s6, s16, 0x1c30ff00
	s_addc_u32 s7, s17, 0
	v_writelane_b32 v254, s6, 23
	s_nop 1
	v_writelane_b32 v254, s7, 24
	s_add_u32 s6, s16, 0x1ab0ee80
	s_addc_u32 s7, s17, 0
	v_writelane_b32 v254, s6, 25
	s_nop 1
	v_writelane_b32 v254, s7, 26
	s_add_u32 s6, s16, 0x1e310780
	s_addc_u32 s7, s17, 0
	v_writelane_b32 v254, s6, 27
	s_cmp_lt_i32 s3, 0
	s_nop 0
	v_writelane_b32 v254, s7, 28
	s_mul_i32 s6, s3, 33
	s_cselect_b32 s4, s6, s4
	s_mulk_i32 s3, 0x81
	s_cselect_b32 s3, s3, s5
	s_add_i32 s4, s4, s2
	s_ashr_i32 s5, s4, 31
	s_lshr_b32 s5, s5, 26
	s_add_i32 s5, s4, s5
	s_and_b32 s6, s5, 0xffc0
	s_sub_i32 s4, s4, s6
	s_bfe_i32 s6, s4, 0x80000
	s_bfe_u32 s6, s6, 0x3000c
	s_add_i32 s6, s4, s6
	s_and_b32 s7, s6, 0xf8
	s_add_i32 s2, s3, s2
	s_sub_i32 s4, s4, s7
	s_ashr_i32 s3, s2, 31
	s_sext_i32_i8 s4, s4
	s_lshl_b32 s5, s5, 5
	s_lshr_b32 s3, s3, 24
	s_and_b32 s5, s5, 0xfffff800
	s_lshl_b32 s4, s4, 8
	s_add_i32 s3, s2, s3
	s_add_i32 s7, s4, s5
	s_and_b32 s4, s3, 0xff00
	s_sub_i32 s2, s2, s4
	s_sext_i32_i16 s4, s2
	s_bfe_u32 s4, s4, 0x3001c
	s_add_i32 s4, s2, s4
	s_and_b32 s5, s4, 0xfff8
	s_sub_i32 s2, s2, s5
	s_sext_i32_i16 s2, s2
	s_lshl_b32 s3, s3, 3
	s_and_b32 s3, s3, 0xfffff800
	s_lshl_b32 s2, s2, 8
	s_add_i32 s5, s2, s3
	s_bfe_i32 s2, s6, 0x80000
	s_sext_i32_i16 s2, s2
	s_ashr_i32 s3, s2, 3
	s_lshr_b32 s2, s2, 3
	v_writelane_b32 v254, s3, 29
	s_bfe_i64 s[2:3], s[2:3], 0x100000
	s_lshl_b64 s[2:3], s[2:3], 20
	v_writelane_b32 v254, s2, 30
	s_nop 1
	v_writelane_b32 v254, s3, 31
	s_sext_i32_i16 s2, s4
	s_ashr_i32 s3, s2, 3
	s_lshr_b32 s2, s2, 3
	v_writelane_b32 v254, s3, 32
	s_bfe_i64 s[2:3], s[2:3], 0x100000
	s_lshl_b64 s[2:3], s[2:3], 20
	v_writelane_b32 v254, s2, 33
	s_nop 1
	v_writelane_b32 v254, s3, 34
	v_writelane_b32 v254, s7, 35
	s_or_b32 s2, s7, 0x80
	v_writelane_b32 v254, s2, 36
	v_writelane_b32 v254, s5, 37
	s_or_b32 s2, s5, 0x80
	v_writelane_b32 v254, s2, 38
	s_lshl_b32 s2, s20, 5
	v_writelane_b32 v254, s2, 39
	s_lshl_b32 s2, s96, 12
	v_writelane_b32 v254, s2, 40
	s_lshl_b32 s2, s20, 12
	v_writelane_b32 v254, s2, 41
	s_lshl_b32 s2, s20, 4
	v_writelane_b32 v254, s2, 42
	v_writelane_b32 v254, s8, 43
	s_or_b32 s2, s8, 1
	v_writelane_b32 v254, s2, 44
	s_add_u32 s2, s16, 0x100c00
	s_addc_u32 s3, s17, 0
	v_writelane_b32 v254, s2, 45
	s_ashr_i32 s89, s88, 31
	s_nop 0
	v_writelane_b32 v254, s3, 46
	v_readlane_b32 s2, v251, 29
	v_readlane_b32 s3, v251, 30
	s_ashr_i32 s3, s2, 31
	v_writelane_b32 v251, s2, 29
	s_nop 1
	v_writelane_b32 v251, s3, 30
	s_mov_b32 s2, 1
	v_writelane_b32 v254, s2, 47
	s_add_i32 s2, 0, 0x19a00
	v_writelane_b32 v254, s2, 48
	s_add_i32 s2, 0, 0x13200
	v_writelane_b32 v254, s2, 49
	s_add_i32 s2, 0, 0x17600
	v_writelane_b32 v254, s2, 50
	s_add_i32 s2, 0, 0x20080
	v_writelane_b32 v254, s2, 51
	s_add_i32 s2, 0, 0x20120
	v_writelane_b32 v254, s2, 52
	s_add_i32 s2, 0, 0x201c0
	v_writelane_b32 v254, s2, 53
	v_cmp_eq_u32_e64 s[2:3], 0, v0
	s_nop 1
	v_writelane_b32 v254, s2, 54
	s_nop 1
	v_writelane_b32 v254, s3, 55
	s_lshl_b64 s[2:3], s[88:89], 12
	v_writelane_b32 v254, s2, 56
	s_nop 1
	v_writelane_b32 v254, s3, 57
	s_lshl_b64 s[2:3], s[88:89], 13
	v_writelane_b32 v254, s2, 58
	s_nop 1
	v_writelane_b32 v254, s3, 59
	s_mov_b64 s[2:3], s[16:17]
	v_writelane_b32 v254, s2, 60
	s_nop 1
	v_writelane_b32 v254, s3, 61
	v_writelane_b32 v254, s66, 62
	s_mov_b32 s2, s88
	v_writelane_b32 v254, s2, 63
	s_nop 1
	v_writelane_b32 v250, s3, 0
	v_writelane_b32 v250, s78, 1
	s_nop 1
	v_writelane_b32 v250, s79, 2
	v_writelane_b32 v250, s96, 3
	s_nop 1
	v_writelane_b32 v250, s97, 4
	v_writelane_b32 v250, s26, 5
	s_nop 1
	v_writelane_b32 v250, s27, 6
	s_branch .LBB0_106
.LBB0_104:
	s_or_b64 exec, exec, s[2:3]
	s_waitcnt lgkmcnt(0)
	s_barrier

.LBB0_170:
	v_readlane_b32 s4, v253, 8
	v_readlane_b32 s5, v253, 9
	v_cvt_f32_u32_e32 v1, v4
	v_sub_u32_e32 v6, 0, v4
	v_rcp_iflag_f32_e32 v1, v1
	s_nop 1
	global_atomic_add v5, v3, v228, s[4:5] sc0
	buffer_inv sc1
	v_mul_f32_e32 v1, 0x4f7ffffe, v1
	v_cvt_u32_f32_e32 v1, v1
	v_mul_lo_u32 v6, v6, v1
	v_mul_hi_u32 v6, v1, v6
	v_add_u32_e32 v1, v1, v6
	s_waitcnt vmcnt(1)
	v_mul_hi_u32 v1, v5, v1
	v_mul_lo_u32 v6, v1, v4
	v_sub_u32_e32 v6, v5, v6
	v_add_u32_e32 v7, 1, v1
	v_cmp_ge_u32_e32 vcc, v6, v4
	v_add_u32_e32 v5, 1, v5
	s_nop 0
	v_cndmask_b32_e32 v1, v1, v7, vcc
	v_sub_u32_e32 v7, v6, v4
	v_cndmask_b32_e32 v6, v6, v7, vcc
	v_add_u32_e32 v7, 1, v1
	v_cmp_ge_u32_e32 vcc, v6, v4
	s_nop 1
	v_cndmask_b32_e32 v1, v1, v7, vcc
	v_mul_lo_u32 v6, v4, v1
	v_add_u32_e32 v4, v6, v4
	v_cmp_ne_u32_e32 vcc, v5, v4
	v_sub_u32_e32 v7, v4, v6
	v_add_u32_e32 v1, 1, v1
	v_lshlrev_b32_e32 v1, 8, v1
	v_readlane_b32 s6, v253, 10
	v_readlane_b32 s7, v253, 11
	s_waitcnt lgkmcnt(0)
	s_cbranch_vccnz .Lnb_poll_0
	buffer_wbl2 sc1
	s_add_u32 s12, s16, 0x6400
	s_addc_u32 s13, s17, 0
	s_mov_b32 s14, 16
	s_waitcnt vmcnt(0)
.Lnb_loop_0:
	global_atomic_add v3, v7, s[12:13]
	s_add_u32 s12, s12, 0x100
	s_addc_u32 s13, s13, 0
	s_sub_u32 s14, s14, 1
	s_cmp_lg_u32 s14, 0
	s_cbranch_scc1 .Lnb_loop_0
.Lnb_poll_0:
	s_mov_b32 s14, 0
	s_nop 4
.Lnb_spin_0:
	global_load_dword v2, v3, s[6:7] sc1
	s_waitcnt vmcnt(0)
	v_sub_u32_e32 v2, v2, v1
	v_cmp_gt_i32_e32 vcc, 0, v2
	s_cbranch_vccz .Lnb_done_0
	s_sleep 1
	s_add_u32 s14, s14, 1
	s_cmp_lt_u32 s14, 0x20000
	s_cbranch_scc1 .Lnb_spin_0

.Lnb_done_10:
	s_getpc_b64 s[98:99]
